# v103 + nt (streaming) hint on the P2 chunk-state flush stores
# baseline (speedup 1.0000x reference)
.Lp2_nofl_a:
	s_bitcmp0_b32 s62, 0
	s_cselect_b64 s[40:41], -1, 0
	s_and_b64 s[42:43], s[40:41], exec
	s_cselect_b32 s42, s52, s53
	v_mov_b32_e32 v52, s26
	v_add3_u32 v53, s42, v92, v93
	ds_read_b32 v52, v52 offset:4604
	ds_read_b128 v[120:123], v53
	ds_read_b128 v[124:127], v53 offset:64
	ds_read_b128 v[128:131], v53 offset:4352
	ds_read_b128 v[132:135], v53 offset:4416
	ds_read_b128 v[136:139], v53 offset:8704
	ds_read_b128 v[140:143], v53 offset:8768
	ds_read_b128 v[144:147], v53 offset:13056
	ds_read_b128 v[148:151], v53 offset:13120
	s_waitcnt lgkmcnt(7)
	v_mfma_f32_16x16x32_bf16 v[120:123], v[14:17], v[120:123], 0
	s_waitcnt lgkmcnt(5)
	v_mfma_f32_16x16x32_bf16 v[128:131], v[14:17], v[128:131], 0
	s_waitcnt lgkmcnt(3)
	v_mfma_f32_16x16x32_bf16 v[136:139], v[14:17], v[136:139], 0
	s_waitcnt lgkmcnt(1)
	v_mfma_f32_16x16x32_bf16 v[144:147], v[14:17], v[144:147], 0
	s_cmp_eq_u32 s62, 0
	s_cbranch_scc1 .Lp2_nost_a
	global_store_dwordx4 v[206:207], v[198:201], off nt
	global_store_dwordx4 v[206:207], v[202:205], off offset:1024 nt

.LBB0_405:
	s_and_b32 s76, s62, 1
	s_xor_b32 s76, s76, 1
	s_mul_i32 s76, s76, 0x4400
	v_add_u32_e32 v216, s76, v213
	ds_read_b128 v[198:201], v216
	ds_read_b128 v[202:205], v216 offset:1088
	v_lshl_add_u64 v[206:207], s[92:93], 0, v[44:45]
	v_lshl_add_u64 v[206:207], v[206:207], 0, v[214:215]
	s_mov_b32 s76, 0x5dffb000
	s_mov_b32 s77, 0
	v_lshl_add_u64 v[206:207], v[206:207], 0, s[76:77]
	v_add_u32_e32 v19, v94, v93
	ds_read_b32 v18, v21 offset:8188
	ds_read_b128 v[30:33], v19 offset:60416
	ds_read_b128 v[34:37], v19 offset:60480
	ds_read_b128 v[38:41], v19 offset:64768
	ds_read_b128 v[42:45], v19 offset:64832
	ds_read_b128 v[46:49], v107 offset:60416
	ds_read_b128 v[50:53], v107 offset:60480
	ds_read_b128 v[54:57], v108 offset:60416
	ds_read_b128 v[112:115], v108 offset:60480
	s_or_b32 s12, s60, s56
	s_ashr_i32 s13, s12, 31
	s_lshl_b64 s[12:13], s[12:13], 12
	v_mov_b32_e32 v129, s13
	v_or_b32_e32 v20, s12, v22
	s_waitcnt lgkmcnt(7)
	v_mfma_f32_16x16x32_bf16 v[30:33], v[14:17], v[30:33], 0
	s_waitcnt lgkmcnt(5)
	v_mfma_f32_16x16x32_bf16 v[38:41], v[14:17], v[38:41], 0
	s_waitcnt lgkmcnt(3)
	v_mfma_f32_16x16x32_bf16 v[46:49], v[14:17], v[46:49], 0
	s_waitcnt lgkmcnt(1)
	v_mfma_f32_16x16x32_bf16 v[14:17], v[14:17], v[54:57], 0
	global_store_dwordx4 v[206:207], v[198:201], off nt
	global_store_dwordx4 v[206:207], v[202:205], off offset:1024 nt
	ds_read_b128 v[54:57], v19 offset:60544
	ds_read_b128 v[116:119], v19 offset:64896
	ds_read_b128 v[120:123], v107 offset:60544
	ds_read_b128 v[124:127], v108 offset:60544
	v_mfma_f32_16x16x32_bf16 v[30:33], v[10:13], v[34:37], v[30:33]
	v_mfma_f32_16x16x32_bf16 v[34:37], v[10:13], v[42:45], v[38:41]
	v_mfma_f32_16x16x32_bf16 v[38:41], v[10:13], v[50:53], v[46:49]
	s_waitcnt lgkmcnt(4)
	v_mfma_f32_16x16x32_bf16 v[10:13], v[10:13], v[112:115], v[14:17]
	s_nop 2
	ds_read_b128 v[14:17], v19 offset:60608
	ds_read_b128 v[42:45], v19 offset:64960
	ds_read_b128 v[46:49], v107 offset:60608
	ds_read_b128 v[50:53], v108 offset:60608
	s_waitcnt lgkmcnt(7)
	v_mfma_f32_16x16x32_bf16 v[30:33], v[6:9], v[54:57], v[30:33]
	s_waitcnt lgkmcnt(6)
	v_mfma_f32_16x16x32_bf16 v[34:37], v[6:9], v[116:119], v[34:37]
	s_waitcnt lgkmcnt(5)
	v_mfma_f32_16x16x32_bf16 v[38:41], v[6:9], v[120:123], v[38:41]
	s_waitcnt lgkmcnt(4)
	v_mfma_f32_16x16x32_bf16 v[6:9], v[6:9], v[124:127], v[10:13]
	s_waitcnt lgkmcnt(3)
	v_mfma_f32_16x16x32_bf16 v[10:13], v[2:5], v[14:17], v[30:33]
	s_waitcnt lgkmcnt(2)
	v_mfma_f32_16x16x32_bf16 v[14:17], v[2:5], v[42:45], v[34:37]
	s_waitcnt lgkmcnt(1)
	v_mfma_f32_16x16x32_bf16 v[30:33], v[2:5], v[46:49], v[38:41]
	s_waitcnt lgkmcnt(0)
	v_mfma_f32_16x16x32_bf16 v[2:5], v[2:5], v[50:53], v[6:9]
	s_or_b32 s26, s57, 7
	v_lshl_or_b32 v128, s26, 6, v20
	s_nop 0
	v_lshlrev_b64 v[8:9], 8, v[128:129]
	v_lshl_add_u64 v[8:9], v[24:25], 0, v[8:9]
	s_movk_i32 s12, 0x1000
	v_cvt_pk_bf16_f32 v6, v10, v11
	v_add_co_u32_e32 v10, vcc, s12, v8
	v_cvt_pk_bf16_f32 v7, v12, v13
	global_store_dwordx2 v[8:9], v[6:7], off
	s_nop 0
	v_addc_co_u32_e32 v11, vcc, 0, v9, vcc
	v_cvt_pk_bf16_f32 v6, v14, v15
	v_cvt_pk_bf16_f32 v7, v16, v17
	global_store_dwordx2 v[10:11], v[6:7], off
	v_add_co_u32_e32 v10, vcc, 0x2000, v8
	v_cvt_pk_bf16_f32 v6, v30, v31
	v_cvt_pk_bf16_f32 v7, v32, v33
	s_nop 1
	v_addc_co_u32_e32 v11, vcc, 0, v9, vcc
	global_store_dwordx2 v[10:11], v[6:7], off
	v_cvt_pk_bf16_f32 v2, v2, v3
	v_cvt_pk_bf16_f32 v3, v4, v5
	v_add_co_u32_e32 v4, vcc, 0x3000, v8
	s_nop 1
	v_addc_co_u32_e32 v5, vcc, 0, v9, vcc
	global_store_dwordx2 v[4:5], v[2:3], off
	s_and_saveexec_b64 s[12:13], s[28:29]
	s_cbranch_execz .LBB0_396
	s_lshl_b32 s38, s56, 6
	s_or_b32 s38, s38, s59
	s_or_b32 s38, s38, s26
	v_mul_f32_e32 v2, 0x3fb8aa3b, v18
	s_ashr_i32 s39, s38, 31
	v_exp_f32_e32 v2, v2
	s_lshl_b64 s[38:39], s[38:39], 2
	s_add_u32 s38, s33, s38
	s_addc_u32 s39, s44, s39
	global_store_dword v21, v2, s[38:39]
	s_branch .LBB0_396
